# baseline (speedup 1.0000x reference)
_Z16sum_layer_kernelPKfS0_Pf:
	s_load_dwordx4 s[4:7], s[0:1], 0x0
	s_load_dwordx2 s[8:9], s[0:1], 0x10
	s_cmp_lt_u32 s2, 0x100
	s_cbranch_scc1 .Lkeep_low_prio
	s_setprio 3
